# agg2 rewritten as single-pass online softmax: el2 embedded in 128B feat2 rows (no per-edge el gather, no logit phase/LDS weight table); agg1 writes the new layout; plus stageA de-serialization
# speedup vs baseline: 1.0282x; 1.0093x over previous
_Z5k_aggILi4ELi128ELi16ELi16ELb0EEvPKiPKtPKDF16_PKfS7_S7_PvS5_S7_S7_PDF16_PfSA_:
	v_lshrrev_b32_e32 v10, 6, v0
	v_lshl_or_b32 v33, s2, 2, v10
	s_movk_i32 s2, 0x30d4
	v_cmp_gt_i32_e32 vcc, s2, v33
	s_and_saveexec_b64 s[2:3], vcc
	s_cbranch_execz .LBB3_37
	s_load_dwordx8 s[16:23], s[0:1], 0x0
	v_bfe_u32 v35, v0, 4, 2
	v_lshl_or_b32 v12, v33, 2, v35
	v_ashrrev_i32_e32 v13, 31, v12
	s_load_dwordx4 s[36:39], s[0:1], 0x20
	s_load_dword s2, s[0:1], 0x68
	s_waitcnt lgkmcnt(0)
	v_lshl_add_u64 v[2:3], v[12:13], 2, s[16:17]
	global_load_dwordx2 v[42:43], v[2:3], off
	v_and_b32_e32 v58, 15, v0
	v_lshlrev_b32_e32 v1, 5, v58
	s_lshl_b32 s33, s2, 2
	global_load_dwordx4 v[2:5], v1, s[38:39] offset:16
	global_load_dwordx4 v[6:9], v1, s[38:39]
	v_add_u32_e32 v1, s33, v33
	v_min_i32_e32 v62, 0x30d3, v1
	v_lshl_or_b32 v14, v62, 2, v35
	v_ashrrev_i32_e32 v15, 31, v14
	v_or_b32_e32 v59, 16, v58
	v_or_b32_e32 v60, 32, v58
	v_or_b32_e32 v61, 48, v58
	v_lshl_add_u64 v[14:15], v[14:15], 2, s[16:17]
	global_load_dwordx2 v[94:95], v[14:15], off
	v_lshl_add_u64 v[12:13], v[12:13], 3, s[36:37]
	v_bfe_u32 v63, v0, 2, 2
	v_lshlrev_b32_e32 v30, 4, v58
	s_movk_i32 s39, 0x110
	s_movk_i32 s12, 0x4400
	v_and_b32_e32 v69, 3, v0
	v_lshlrev_b32_e32 v34, 2, v35
	v_lshlrev_b32_e32 v0, 4, v35
	s_movk_i32 s13, 0x88
	s_movk_i32 s38, 0x30d3
	s_lshl_b32 s44, s2, 3
	v_cmp_eq_u32_e64 s[2:3], 1, v63
	v_cmp_eq_u32_e64 s[4:5], 2, v63
	v_cmp_eq_u32_e64 s[6:7], 3, v63
	v_mul_lo_u32 v68, s33, v63
	v_cmp_eq_u32_e64 s[8:9], 0, v35
	v_mov_b32_e32 v31, v30
	s_mov_b32 s45, 0xff800000
	v_mov_b32_e32 v77, 0xff800000
	s_movk_i32 s46, 0x41
	s_mov_b32 s47, 0x3fb8aa3b
	s_movk_i32 s48, 0x80
	v_mov_b32_e32 v78, 3
	v_mov_b32_e32 v79, 8
	v_mov_b32_e32 v81, 0
	v_mov_b32_e32 v82, 0
	s_waitcnt vmcnt(3)
	v_add_u32_e32 v1, -1, v43
	v_add_u32_e32 v11, v42, v58
	v_add_u32_e32 v14, v59, v42
	v_add_u32_e32 v15, v60, v42
	v_add_u32_e32 v16, v61, v42
	v_min_i32_e32 v11, v11, v1
	v_min_i32_e32 v14, v14, v1
	v_min_i32_e32 v15, v15, v1
	v_min_i32_e32 v1, v16, v1
	v_max_i32_e32 v11, 0, v11
	v_max_i32_e32 v14, 0, v14
	v_max_i32_e32 v15, 0, v15
	v_max_i32_e32 v1, 0, v1
	v_lshlrev_b32_e32 v11, 1, v11
	v_lshlrev_b32_e32 v14, 1, v14
	v_lshlrev_b32_e32 v15, 1, v15
	v_lshlrev_b32_e32 v1, 1, v1
	global_load_ushort v70, v11, s[18:19]
	global_load_ushort v72, v14, s[18:19]
	global_load_ushort v71, v15, s[18:19]
	global_load_ushort v73, v1, s[18:19]
	global_load_dwordx2 v[26:27], v[12:13], off
	s_load_dwordx4 s[40:43], s[0:1], 0x58
	s_load_dwordx8 s[24:31], s[0:1], 0x38
	s_movk_i32 s0, 0x1100
	s_movk_i32 s1, 0x440
	v_mul_u32_u24_e32 v1, 0x440, v35
	v_mul_u32_u24_e32 v13, 0x110, v35
	v_mul_u32_u24_e32 v11, 0x1100, v10
	v_mad_u32_u24 v12, v10, s0, v1
	v_mad_u32_u24 v10, v10, s1, v13
	v_lshlrev_b32_e32 v13, 2, v58
	v_mov_b32_e32 v1, 0
	v_add_u32_e32 v64, 0x8800, v10
	v_mad_u32_u24 v65, v63, s39, v12
	v_or_b32_e32 v67, v12, v13
	v_or_b32_e32 v12, v11, v30
	v_add_u32_e32 v74, 0x8810, v10
	v_mad_u32_u24 v10, v58, s39, v11
	v_add_u32_e32 v66, v64, v13
	v_add_u32_e32 v32, 0x4400, v12
	v_lshlrev_b32_e32 v12, 3, v35
	s_waitcnt lgkmcnt(0)
	s_add_u32 s42, s42, 0x1da1c0
	s_addc_u32 s43, s43, 0
	v_lshl_add_u64 v[36:37], s[26:27], 0, v[0:1]
	v_lshl_add_u64 v[38:39], s[28:29], 0, v[0:1]
	v_or_b32_e32 v13, 32, v34
	v_add3_u32 v76, v10, v0, s12
	v_mbcnt_lo_u32_b32 v0, -1, 0
	v_cmp_gt_u32_e64 s[0:1], 4, v58
	v_cmp_gt_u32_e64 s[10:11], 40, v13
	v_mad_u32_u24 v75, v58, s13, v12
	s_mov_b64 s[26:27], 0
	v_mbcnt_hi_u32_b32 v80, -1, v0
	s_branch .LBB3_4

.LBB3_35:
	s_or_b64 exec, exec, s[14:15]
	v_and_b32_e32 v10, 64, v80
	v_xor_b32_e32 v0, 16, v80
	v_add_u32_e32 v10, 64, v10
	v_cmp_lt_i32_e64 s[14:15], v0, v10
	v_xor_b32_e32 v12, 32, v80
	s_nop 0
	v_cndmask_b32_e64 v0, v80, v0, s[14:15]
	v_lshlrev_b32_e32 v0, 2, v0
	ds_bpermute_b32 v11, v0, v18
	ds_bpermute_b32 v13, v0, v19
	v_cmp_lt_i32_e64 s[14:15], v12, v10
	s_waitcnt lgkmcnt(1)
	v_add_f32_e32 v0, v18, v11
	v_cndmask_b32_e64 v10, v80, v12, s[14:15]
	v_lshlrev_b32_e32 v12, 2, v10
	s_waitcnt lgkmcnt(0)
	v_add_f32_e32 v11, v19, v13
	ds_bpermute_b32 v10, v12, v0
	ds_bpermute_b32 v12, v12, v11
	s_and_b64 s[14:15], s[8:9], s[12:13]
	s_and_saveexec_b64 s[12:13], s[14:15]
	s_cbranch_execz .LBB3_2
	v_ashrrev_i32_e32 v43, 31, v42
	s_waitcnt lgkmcnt(0)
	v_add_f32_e32 v14, v11, v12
	v_add_f32_e32 v0, v0, v10
	v_lshlrev_b64 v[10:11], 1, v[42:43]
	v_fma_mixlo_f16 v0, v0, s47, 0
	global_store_short v[44:45], v0, off offset:80
	v_fma_mixlo_f16 v0, v14, s47, 0
	v_lshl_add_u64 v[10:11], s[42:43], 0, v[10:11]
	global_store_short v[10:11], v0, off
	s_branch .LBB3_2
.LBB3_37:
	s_endpgm
	s_nop 0
	s_nop 0
	s_nop 0
	s_nop 0
	s_nop 0
	s_nop 0
	s_nop 0
	s_nop 0
	s_nop 0
	s_endpgm

_Z5k_aggILi1ELi40ELi5ELi5ELb1EEvPKiPKtPKDF16_PKfS7_S7_PvS5_S7_S7_PDF16_PfSA_:
	v_lshrrev_b32_e32 v46, 6, v0
	s_lshl_b32 s3, s2, 2
	v_readfirstlane_b32 s25, v46
	s_load_dwordx4 s[4:7], s[0:1], 0x0
	s_load_dwordx2 s[8:9], s[0:1], 0x10
	s_load_dwordx2 s[12:13], s[0:1], 0x20
	s_load_dwordx4 s[16:19], s[0:1], 0x28
	s_load_dword s20, s[0:1], 0x68
	s_add_i32 s25, s25, s3
	s_cmpk_ge_i32 s25, 0x30d4
	s_cbranch_scc1 .Lagg2n_end
	v_and_b32_e32 v52, 15, v0
	v_bfe_u32 v53, v0, 4, 2
	v_lshrrev_b32_e32 v54, 3, v52
	v_and_b32_e32 v55, 7, v52
	v_min_u32_e32 v47, 5, v55
	v_lshlrev_b32_e32 v56, 4, v47
	v_lshl_or_b32 v47, v46, 2, v53
	v_mul_u32_u24_e32 v47, 0x110, v47
	v_lshl_add_u32 v57, v52, 2, v47
	v_lshl_add_u32 v58, v54, 4, v47
	v_cmp_gt_u32_e32 vcc, 5, v52
	v_min_u32_e32 v47, 4, v55
	v_lshlrev_b32_e32 v47, 5, v47
	s_mov_b64 s[26:27], vcc
	v_mov_b32_e32 v51, 0xff800000
	s_waitcnt lgkmcnt(0)
	s_add_u32 s12, s12, 0x1da1c0
	s_addc_u32 s13, s13, 0
	s_lshl_b32 s11, s20, 2
	global_load_dwordx4 v[34:37], v47, s[16:17]
	global_load_dwordx4 v[38:41], v47, s[16:17] offset:16
	v_lshl_or_b32 v59, s25, 2, v53
	v_lshlrev_b32_e32 v47, 2, v59
	global_load_dwordx2 v[60:61], v47, s[4:5]
	s_add_i32 s28, s25, s11
	s_min_i32 s28, s28, 0x30d3
	v_lshl_or_b32 v48, s28, 2, v53
	v_lshlrev_b32_e32 v47, 2, v48
	global_load_dwordx2 v[62:63], v47, s[4:5]
	v_lshlrev_b32_e32 v47, 1, v59
	global_load_ushort v70, v47, s[12:13]
	s_waitcnt vmcnt(2)
	v_add_u32_e32 v46, -1, v61
	v_add_u32_e32 v47, v60, v52
	v_min_i32_e32 v48, v47, v46
	v_max_i32_e32 v48, 0, v48
	v_lshlrev_b32_e32 v48, 1, v48
	global_load_ushort v66, v48, s[6:7]
	v_add_u32_e32 v48, 16, v47
	v_min_i32_e32 v48, v48, v46
	v_max_i32_e32 v48, 0, v48
	v_lshlrev_b32_e32 v48, 1, v48
	global_load_ushort v67, v48, s[6:7]
	v_add_u32_e32 v48, 32, v47
	v_min_i32_e32 v48, v48, v46
	v_max_i32_e32 v48, 0, v48
	v_lshlrev_b32_e32 v48, 1, v48
	global_load_ushort v68, v48, s[6:7]
	v_add_u32_e32 v48, 48, v47
	v_min_i32_e32 v48, v48, v46
	v_max_i32_e32 v48, 0, v48
	v_lshlrev_b32_e32 v48, 1, v48
	global_load_ushort v69, v48, s[6:7]
	s_waitcnt vmcnt(0)
.Lagg2n_quad:
	v_cvt_f32_f16_e32 v71, v70
	v_lshlrev_b32_e32 v46, 7, v66
	v_lshlrev_b32_e32 v47, 7, v67
	v_lshlrev_b32_e32 v48, 7, v68
	v_lshlrev_b32_e32 v49, 7, v69
	ds_write2_b32 v57, v46, v47 offset1:16
	ds_write2_b32 v57, v48, v49 offset0:32 offset1:48
	v_sub_u32_e32 v72, v61, v60
	s_add_i32 s28, s25, s11
	s_add_i32 s29, s28, s11
	s_min_i32 s28, s28, 0x30d3
	s_min_i32 s29, s29, 0x30d3
	v_lshl_or_b32 v46, s29, 2, v53
	v_lshlrev_b32_e32 v46, 2, v46
	global_load_dwordx2 v[64:65], v46, s[4:5]
	v_add_u32_e32 v46, -1, v63
	v_add_u32_e32 v47, v62, v52
	v_min_i32_e32 v48, v47, v46
	v_max_i32_e32 v48, 0, v48
	v_lshlrev_b32_e32 v48, 1, v48
	global_load_ushort v66, v48, s[6:7]
	v_add_u32_e32 v48, 16, v47
	v_min_i32_e32 v48, v48, v46
	v_max_i32_e32 v48, 0, v48
	v_lshlrev_b32_e32 v48, 1, v48
	global_load_ushort v67, v48, s[6:7]
	v_add_u32_e32 v48, 32, v47
	v_min_i32_e32 v48, v48, v46
	v_max_i32_e32 v48, 0, v48
	v_lshlrev_b32_e32 v48, 1, v48
	global_load_ushort v68, v48, s[6:7]
	v_add_u32_e32 v48, 48, v47
	v_min_i32_e32 v48, v48, v46
	v_max_i32_e32 v48, 0, v48
	v_lshlrev_b32_e32 v48, 1, v48
	global_load_ushort v69, v48, s[6:7]
	v_lshl_or_b32 v46, s28, 2, v53
	v_lshlrev_b32_e32 v46, 1, v46
	global_load_ushort v70, v46, s[12:13]
	v_readlane_b32 s30, v72, 0
	v_readlane_b32 s31, v72, 16
	v_readlane_b32 s32, v72, 32
	v_readlane_b32 s33, v72, 48
	v_mov_b32_e32 v24, 0
	v_mov_b32_e32 v25, 0
	v_mov_b32_e32 v26, 0
	v_mov_b32_e32 v27, 0
	v_mov_b32_e32 v28, 0
	v_mov_b32_e32 v29, 0
	v_mov_b32_e32 v30, 0
	v_mov_b32_e32 v31, 0
	v_mov_b32_e32 v32, 0
	v_mov_b32_e32 v33, 0xff800000
	s_max_i32 s30, s30, s31
	s_max_i32 s32, s32, s33
	s_max_i32 s21, s30, s32
	s_mov_b32 s22, 0
.Lagg2n_pass:
	v_subrev_u32_e32 v73, s22, v72
	v_med3_i32 v73, v73, 0, 64
	v_lshlrev_b32_e32 v46, 2, v54
	v_sub_u32_e32 v74, v73, v46
	s_sub_i32 s28, s21, s22
	s_min_i32 s28, s28, 64
	s_add_i32 s28, s28, 7
	s_lshr_b32 s23, s28, 3
	s_mov_b32 s24, 0
	v_mov_b32_e32 v75, v58
.Lagg2n_stage:
	ds_read_b128 v[42:45], v75
	s_waitcnt lgkmcnt(0)
	v_add_u32_e32 v42, v42, v56
	v_add_u32_e32 v43, v43, v56
	v_add_u32_e32 v44, v44, v56
	v_add_u32_e32 v45, v45, v56
	global_load_dwordx4 v[0:3], v42, s[8:9]
	global_load_dwordx4 v[4:7], v43, s[8:9]
	global_load_dwordx4 v[8:11], v44, s[8:9]
	global_load_dwordx4 v[12:15], v45, s[8:9]
	s_waitcnt vmcnt(0)
	ds_swizzle_b32 v16, v0 offset:0xb8
	ds_swizzle_b32 v17, v4 offset:0xb8
	ds_swizzle_b32 v18, v8 offset:0xb8
	ds_swizzle_b32 v19, v12 offset:0xb8
	s_waitcnt lgkmcnt(0)
	v_cvt_f32_f16_e32 v16, v16
	v_cvt_f32_f16_e32 v17, v17
	v_cvt_f32_f16_e32 v18, v18
	v_cvt_f32_f16_e32 v19, v19
	v_add_f32_e32 v16, v16, v71
	v_add_f32_e32 v17, v17, v71
	v_add_f32_e32 v18, v18, v71
	v_add_f32_e32 v19, v19, v71
	v_mul_f32_e32 v46, 0x3e4ccccd, v16
	v_mul_f32_e32 v47, 0x3e4ccccd, v17
	v_mul_f32_e32 v48, 0x3e4ccccd, v18
	v_mul_f32_e32 v49, 0x3e4ccccd, v19
	v_max_f32_e32 v16, v16, v46
	v_max_f32_e32 v17, v17, v47
	v_max_f32_e32 v18, v18, v48
	v_max_f32_e32 v19, v19, v49
	v_cmp_lt_i32_e64 s[28:29], 0, v74
	v_cmp_lt_i32_e64 s[30:31], 1, v74
	v_cmp_lt_i32_e64 s[32:33], 2, v74
	v_cmp_lt_i32_e64 s[34:35], 3, v74
	v_cndmask_b32_e64 v16, v51, v16, s[28:29]
	v_cndmask_b32_e64 v17, v51, v17, s[30:31]
	v_cndmask_b32_e64 v18, v51, v18, s[32:33]
	v_cndmask_b32_e64 v19, v51, v19, s[34:35]
	v_max3_f32 v46, v16, v17, v18
	v_max_f32_e32 v46, v46, v19
	s_nop 1
	v_mov_b32_dpp v47, v46 row_ror:8 row_mask:0xf bank_mask:0xf
	v_max_f32_e32 v46, v46, v47
	v_max_f32_e32 v47, v33, v46
	v_cmp_neq_f32_e32 vcc, 0xff800000, v47
	v_sub_f32_e32 v20, v16, v47
	v_sub_f32_e32 v21, v17, v47
	v_cndmask_b32_e32 v46, 0, v47, vcc
	v_sub_f32_e32 v48, v33, v46
	v_sub_f32_e32 v20, v16, v46
	v_sub_f32_e32 v21, v17, v46
	v_sub_f32_e32 v22, v18, v46
	v_sub_f32_e32 v23, v19, v46
	v_exp_f32_e32 v48, v48
	v_exp_f32_e32 v20, v20
	v_exp_f32_e32 v21, v21
	v_exp_f32_e32 v22, v22
	v_exp_f32_e32 v23, v23
	v_mov_b32_e32 v33, v46
	v_mul_f32_e32 v24, v24, v48
	v_mul_f32_e32 v25, v25, v48
	v_mul_f32_e32 v26, v26, v48
	v_mul_f32_e32 v27, v27, v48
	v_mul_f32_e32 v28, v28, v48
	v_mul_f32_e32 v29, v29, v48
	v_mul_f32_e32 v30, v30, v48
	v_mul_f32_e32 v31, v31, v48
	v_mul_f32_e32 v32, v32, v48
	v_fma_mix_f32 v24, v0, v20, v24 op_sel_hi:[1,0,0]
	v_fma_mix_f32 v25, v0, v20, v25 op_sel:[1,0,0] op_sel_hi:[1,0,0]
	v_fma_mix_f32 v26, v1, v20, v26 op_sel_hi:[1,0,0]
	v_fma_mix_f32 v27, v1, v20, v27 op_sel:[1,0,0] op_sel_hi:[1,0,0]
	v_fma_mix_f32 v28, v2, v20, v28 op_sel_hi:[1,0,0]
	v_fma_mix_f32 v29, v2, v20, v29 op_sel:[1,0,0] op_sel_hi:[1,0,0]
	v_fma_mix_f32 v30, v3, v20, v30 op_sel_hi:[1,0,0]
	v_fma_mix_f32 v31, v3, v20, v31 op_sel:[1,0,0] op_sel_hi:[1,0,0]
	v_fma_mix_f32 v24, v4, v21, v24 op_sel_hi:[1,0,0]
	v_fma_mix_f32 v25, v4, v21, v25 op_sel:[1,0,0] op_sel_hi:[1,0,0]
	v_fma_mix_f32 v26, v5, v21, v26 op_sel_hi:[1,0,0]
	v_fma_mix_f32 v27, v5, v21, v27 op_sel:[1,0,0] op_sel_hi:[1,0,0]
	v_fma_mix_f32 v28, v6, v21, v28 op_sel_hi:[1,0,0]
	v_fma_mix_f32 v29, v6, v21, v29 op_sel:[1,0,0] op_sel_hi:[1,0,0]
	v_fma_mix_f32 v30, v7, v21, v30 op_sel_hi:[1,0,0]
	v_fma_mix_f32 v31, v7, v21, v31 op_sel:[1,0,0] op_sel_hi:[1,0,0]
	v_fma_mix_f32 v24, v8, v22, v24 op_sel_hi:[1,0,0]
	v_fma_mix_f32 v25, v8, v22, v25 op_sel:[1,0,0] op_sel_hi:[1,0,0]
	v_fma_mix_f32 v26, v9, v22, v26 op_sel_hi:[1,0,0]
	v_fma_mix_f32 v27, v9, v22, v27 op_sel:[1,0,0] op_sel_hi:[1,0,0]
	v_fma_mix_f32 v28, v10, v22, v28 op_sel_hi:[1,0,0]
	v_fma_mix_f32 v29, v10, v22, v29 op_sel:[1,0,0] op_sel_hi:[1,0,0]
	v_fma_mix_f32 v30, v11, v22, v30 op_sel_hi:[1,0,0]
	v_fma_mix_f32 v31, v11, v22, v31 op_sel:[1,0,0] op_sel_hi:[1,0,0]
	v_fma_mix_f32 v24, v12, v23, v24 op_sel_hi:[1,0,0]
	v_fma_mix_f32 v25, v12, v23, v25 op_sel:[1,0,0] op_sel_hi:[1,0,0]
	v_fma_mix_f32 v26, v13, v23, v26 op_sel_hi:[1,0,0]
	v_fma_mix_f32 v27, v13, v23, v27 op_sel:[1,0,0] op_sel_hi:[1,0,0]
	v_fma_mix_f32 v28, v14, v23, v28 op_sel_hi:[1,0,0]
	v_fma_mix_f32 v29, v14, v23, v29 op_sel:[1,0,0] op_sel_hi:[1,0,0]
	v_fma_mix_f32 v30, v15, v23, v30 op_sel_hi:[1,0,0]
	v_fma_mix_f32 v31, v15, v23, v31 op_sel:[1,0,0] op_sel_hi:[1,0,0]
	v_add_f32_e32 v46, v20, v21
	v_add_f32_e32 v47, v22, v23
	v_add_f32_e32 v46, v46, v47
	v_add_f32_e32 v32, v32, v46
	v_add_u32_e32 v75, 32, v75
	v_add_u32_e32 v74, -8, v74
	s_add_i32 s24, s24, 1
	s_cmp_lt_i32 s24, s23
	s_cbranch_scc1 .Lagg2n_stage
	s_add_i32 s22, s22, 64
	s_cmp_lt_i32 s22, s21
	s_cbranch_scc0 .Lagg2n_epi
	v_add_u32_e32 v46, -1, v61
	v_add_u32_e32 v47, v60, v52
	v_add_u32_e32 v47, s22, v47
	v_min_i32_e32 v48, v47, v46
	v_max_i32_e32 v48, 0, v48
	v_lshlrev_b32_e32 v48, 1, v48
	global_load_ushort v42, v48, s[6:7]
	v_add_u32_e32 v48, 16, v47
	v_min_i32_e32 v48, v48, v46
	v_max_i32_e32 v48, 0, v48
	v_lshlrev_b32_e32 v48, 1, v48
	global_load_ushort v43, v48, s[6:7]
	v_add_u32_e32 v48, 32, v47
	v_min_i32_e32 v48, v48, v46
	v_max_i32_e32 v48, 0, v48
	v_lshlrev_b32_e32 v48, 1, v48
	global_load_ushort v44, v48, s[6:7]
	v_add_u32_e32 v48, 48, v47
	v_min_i32_e32 v48, v48, v46
	v_max_i32_e32 v48, 0, v48
	v_lshlrev_b32_e32 v48, 1, v48
	global_load_ushort v45, v48, s[6:7]
	s_waitcnt vmcnt(0)
	v_lshlrev_b32_e32 v42, 7, v42
	v_lshlrev_b32_e32 v43, 7, v43
	v_lshlrev_b32_e32 v44, 7, v44
	v_lshlrev_b32_e32 v45, 7, v45
	ds_write2_b32 v57, v42, v43 offset1:16
	ds_write2_b32 v57, v44, v45 offset0:32 offset1:48
	s_branch .Lagg2n_pass
.Lagg2n_epi:
	v_add_f32_dpp v24, v24, v24 row_ror:8 row_mask:0xf bank_mask:0xf
	v_add_f32_dpp v25, v25, v25 row_ror:8 row_mask:0xf bank_mask:0xf
	v_add_f32_dpp v26, v26, v26 row_ror:8 row_mask:0xf bank_mask:0xf
	v_add_f32_dpp v27, v27, v27 row_ror:8 row_mask:0xf bank_mask:0xf
	v_add_f32_dpp v28, v28, v28 row_ror:8 row_mask:0xf bank_mask:0xf
	v_add_f32_dpp v29, v29, v29 row_ror:8 row_mask:0xf bank_mask:0xf
	v_add_f32_dpp v30, v30, v30 row_ror:8 row_mask:0xf bank_mask:0xf
	v_add_f32_dpp v31, v31, v31 row_ror:8 row_mask:0xf bank_mask:0xf
	v_add_f32_dpp v32, v32, v32 row_ror:8 row_mask:0xf bank_mask:0xf
	v_mov_b32_e32 v60, v62
	v_mov_b32_e32 v61, v63
	v_mov_b32_e32 v62, v64
	v_mov_b32_e32 v63, v65
	v_rcp_f32_e32 v46, v32
	v_cmp_lt_f32_e32 vcc, 0, v32
	v_mul_u32_u24_e32 v47, 0xa0, v59
	v_lshl_add_u32 v47, v55, 5, v47
	v_cndmask_b32_e32 v46, 0, v46, vcc
	v_fma_f32 v0, v24, v46, v34
	v_fma_f32 v1, v25, v46, v35
	v_fma_f32 v2, v26, v46, v36
	v_fma_f32 v3, v27, v46, v37
	v_fma_f32 v4, v28, v46, v38
	v_fma_f32 v5, v29, v46, v39
	v_fma_f32 v6, v30, v46, v40
	v_fma_f32 v7, v31, v46, v41
	s_and_saveexec_b64 s[28:29], s[26:27]
	global_store_dwordx4 v47, v[0:3], s[18:19] nt
	global_store_dwordx4 v47, v[4:7], s[18:19] offset:16 nt
	s_mov_b64 exec, s[28:29]
	s_add_i32 s25, s25, s11
	s_cmpk_ge_i32 s25, 0x30d4
	s_cbranch_scc1 .Lagg2n_end
	v_lshl_or_b32 v59, s25, 2, v53
	s_branch .Lagg2n_quad

	.amdhsa_kernel _Z5k_aggILi1ELi40ELi5ELi5ELb1EEvPKiPKtPKDF16_PKfS7_S7_PvS5_S7_S7_PDF16_PfSA_
		.amdhsa_group_segment_fixed_size 8704
		.amdhsa_private_segment_fixed_size 0
		.amdhsa_kernarg_size 360
		.amdhsa_user_sgpr_count 2
		.amdhsa_user_sgpr_dispatch_ptr 0
		.amdhsa_user_sgpr_queue_ptr 0
		.amdhsa_user_sgpr_kernarg_segment_ptr 1
		.amdhsa_user_sgpr_dispatch_id 0
		.amdhsa_user_sgpr_kernarg_preload_length 0
		.amdhsa_user_sgpr_kernarg_preload_offset 0
		.amdhsa_user_sgpr_private_segment_size 0
		.amdhsa_uses_dynamic_stack 0
		.amdhsa_enable_private_segment 0
		.amdhsa_system_sgpr_workgroup_id_x 1
		.amdhsa_system_sgpr_workgroup_id_y 0
		.amdhsa_system_sgpr_workgroup_id_z 0
		.amdhsa_system_sgpr_workgroup_info 0
		.amdhsa_system_vgpr_workitem_id 0
		.amdhsa_next_free_vgpr 76
		.amdhsa_next_free_sgpr 40
		.amdhsa_accum_offset 76
		.amdhsa_reserve_vcc 1
		.amdhsa_float_round_mode_32 0
		.amdhsa_float_round_mode_16_64 0
		.amdhsa_float_denorm_mode_32 3
		.amdhsa_float_denorm_mode_16_64 3
		.amdhsa_dx10_clamp 1
		.amdhsa_ieee_mode 1
		.amdhsa_fp16_overflow 0
		.amdhsa_tg_split 0
		.amdhsa_exception_fp_ieee_invalid_op 0
		.amdhsa_exception_fp_denorm_src 0
		.amdhsa_exception_fp_ieee_div_zero 0
		.amdhsa_exception_fp_ieee_overflow 0
		.amdhsa_exception_fp_ieee_underflow 0
		.amdhsa_exception_fp_ieee_inexact 0
		.amdhsa_exception_int_div_zero 0
	.end_amdhsa_kernel

amdhsa.kernels:
  - .agpr_count:     0
    .args:
      - .actual_access:  read_only
        .address_space:  global
        .offset:         0
        .size:           8
        .value_kind:     global_buffer
      - .actual_access:  read_only
        .address_space:  global
        .offset:         8
        .size:           8
        .value_kind:     global_buffer
      - .actual_access:  write_only
        .address_space:  global
        .offset:         16
        .size:           8
        .value_kind:     global_buffer
      - .actual_access:  write_only
        .address_space:  global
        .offset:         24
        .size:           8
        .value_kind:     global_buffer
    .group_segment_fixed_size: 32320
    .kernarg_segment_align: 8
    .kernarg_segment_size: 32
    .language:       OpenCL C
    .language_version:
      - 2
      - 0
    .max_flat_workgroup_size: 1024
    .name:           _Z6k_finePKjPKtPiPt
    .private_segment_fixed_size: 0
    .sgpr_count:     71
    .sgpr_spill_count: 0
    .symbol:         _Z6k_finePKjPKtPiPt.kd
    .uniform_work_group_size: 1
    .uses_dynamic_stack: false
    .vgpr_count:     54
    .vgpr_spill_count: 0
    .wavefront_size: 64
  - .agpr_count:     0
    .args:
      - .actual_access:  read_only
        .address_space:  global
        .offset:         0
        .size:           8
        .value_kind:     global_buffer
      - .actual_access:  read_only
        .address_space:  global
        .offset:         8
        .size:           8
        .value_kind:     global_buffer
      - .actual_access:  write_only
        .address_space:  global
        .offset:         16
        .size:           8
        .value_kind:     global_buffer
      - .actual_access:  write_only
        .address_space:  global
        .offset:         24
        .size:           8
        .value_kind:     global_buffer
      - .actual_access:  read_only
        .address_space:  global
        .offset:         32
        .size:           8
        .value_kind:     global_buffer
      - .actual_access:  read_only
        .address_space:  global
        .offset:         40
        .size:           8
        .value_kind:     global_buffer
      - .actual_access:  write_only
        .address_space:  global
        .offset:         48
        .size:           8
        .value_kind:     global_buffer
      - .actual_access:  write_only
        .address_space:  global
        .offset:         56
        .size:           8
        .value_kind:     global_buffer
      - .actual_access:  read_only
        .address_space:  global
        .offset:         64
        .size:           8
        .value_kind:     global_buffer
      - .actual_access:  read_only
        .address_space:  global
        .offset:         72
        .size:           8
        .value_kind:     global_buffer
      - .actual_access:  read_only
        .address_space:  global
        .offset:         80
        .size:           8
        .value_kind:     global_buffer
      - .actual_access:  write_only
        .address_space:  global
        .offset:         88
        .size:           8
        .value_kind:     global_buffer
      - .actual_access:  write_only
        .address_space:  global
        .offset:         96
        .size:           8
        .value_kind:     global_buffer
      - .actual_access:  write_only
        .address_space:  global
        .offset:         104
        .size:           8
        .value_kind:     global_buffer
    .group_segment_fixed_size: 53248
    .kernarg_segment_align: 8
    .kernarg_segment_size: 112
    .language:       OpenCL C
    .language_version:
      - 2
      - 0
    .max_flat_workgroup_size: 256
    .name:           _Z8k_stageAPKiS0_PjPtPKfS4_PDF16_S5_S4_S4_S4_S5_PfS6_
    .private_segment_fixed_size: 0
    .sgpr_count:     75
    .sgpr_spill_count: 0
    .symbol:         _Z8k_stageAPKiS0_PjPtPKfS4_PDF16_S5_S4_S4_S4_S5_PfS6_.kd
    .uniform_work_group_size: 1
    .uses_dynamic_stack: false
    .vgpr_count:     158
    .vgpr_spill_count: 0
    .wavefront_size: 64
  - .agpr_count:     4
    .args:
      - .actual_access:  read_only
        .address_space:  global
        .offset:         0
        .size:           8
        .value_kind:     global_buffer
      - .actual_access:  read_only
        .address_space:  global
        .offset:         8
        .size:           8
        .value_kind:     global_buffer
      - .actual_access:  read_only
        .address_space:  global
        .offset:         16
        .size:           8
        .value_kind:     global_buffer
      - .actual_access:  read_only
        .address_space:  global
        .offset:         24
        .size:           8
        .value_kind:     global_buffer
      - .actual_access:  write_only
        .address_space:  global
        .offset:         32
        .size:           8
        .value_kind:     global_buffer
      - .actual_access:  write_only
        .address_space:  global
        .offset:         40
        .size:           8
        .value_kind:     global_buffer
      - .actual_access:  write_only
        .address_space:  global
        .offset:         48
        .size:           8
        .value_kind:     global_buffer
    .group_segment_fixed_size: 19584
    .kernarg_segment_align: 8
    .kernarg_segment_size: 56
    .language:       OpenCL C
    .language_version:
      - 2
      - 0
    .max_flat_workgroup_size: 256
    .name:           _Z7k_gemm2PKDF16_S0_PKfS2_PDF16_PfS4_
    .private_segment_fixed_size: 0
    .sgpr_count:     30
    .sgpr_spill_count: 0
    .symbol:         _Z7k_gemm2PKDF16_S0_PKfS2_PDF16_PfS4_.kd
    .uniform_work_group_size: 1
    .uses_dynamic_stack: false
    .vgpr_count:     84
    .vgpr_spill_count: 0
    .wavefront_size: 64
  - .agpr_count:     12
    .args:
      - .actual_access:  read_only
        .address_space:  global
        .offset:         0
        .size:           8
        .value_kind:     global_buffer
      - .actual_access:  read_only
        .address_space:  global
        .offset:         8
        .size:           8
        .value_kind:     global_buffer
      - .actual_access:  read_only
        .address_space:  global
        .offset:         16
        .size:           8
        .value_kind:     global_buffer
      - .actual_access:  read_only
        .address_space:  global
        .offset:         24
        .size:           8
        .value_kind:     global_buffer
      - .actual_access:  read_only
        .address_space:  global
        .offset:         32
        .size:           8
        .value_kind:     global_buffer
      - .actual_access:  read_only
        .address_space:  global
        .offset:         40
        .size:           8
        .value_kind:     global_buffer
      - .actual_access:  read_only
        .address_space:  global
        .offset:         48
        .size:           8
        .value_kind:     global_buffer
      - .actual_access:  read_only
        .address_space:  global
        .offset:         56
        .size:           8
        .value_kind:     global_buffer
      - .actual_access:  read_only
        .address_space:  global
        .offset:         64
        .size:           8
        .value_kind:     global_buffer
      - .actual_access:  read_only
        .address_space:  global
        .offset:         72
        .size:           8
        .value_kind:     global_buffer
      - .actual_access:  write_only
        .address_space:  global
        .offset:         80
        .size:           8
        .value_kind:     global_buffer
      - .actual_access:  write_only
        .address_space:  global
        .offset:         88
        .size:           8
        .value_kind:     global_buffer
      - .actual_access:  write_only
        .address_space:  global
        .offset:         96
        .size:           8
        .value_kind:     global_buffer
      - .offset:         104
        .size:           4
        .value_kind:     hidden_block_count_x
      - .offset:         108
        .size:           4
        .value_kind:     hidden_block_count_y
      - .offset:         112
        .size:           4
        .value_kind:     hidden_block_count_z
      - .offset:         116
        .size:           2
        .value_kind:     hidden_group_size_x
      - .offset:         118
        .size:           2
        .value_kind:     hidden_group_size_y
      - .offset:         120
        .size:           2
        .value_kind:     hidden_group_size_z
      - .offset:         122
        .size:           2
        .value_kind:     hidden_remainder_x
      - .offset:         124
        .size:           2
        .value_kind:     hidden_remainder_y
      - .offset:         126
        .size:           2
        .value_kind:     hidden_remainder_z
      - .offset:         144
        .size:           8
        .value_kind:     hidden_global_offset_x
      - .offset:         152
        .size:           8
        .value_kind:     hidden_global_offset_y
      - .offset:         160
        .size:           8
        .value_kind:     hidden_global_offset_z
      - .offset:         168
        .size:           2
        .value_kind:     hidden_grid_dims
    .group_segment_fixed_size: 39168
    .kernarg_segment_align: 8
    .kernarg_segment_size: 360
    .language:       OpenCL C
    .language_version:
      - 2
      - 0
    .max_flat_workgroup_size: 256
    .name:           _Z5k_aggILi4ELi128ELi16ELi16ELb0EEvPKiPKtPKDF16_PKfS7_S7_PvS5_S7_S7_PDF16_PfSA_
    .private_segment_fixed_size: 0
    .sgpr_count:     55
    .sgpr_spill_count: 0
    .symbol:         _Z5k_aggILi4ELi128ELi16ELi16ELb0EEvPKiPKtPKDF16_PKfS7_S7_PvS5_S7_S7_PDF16_PfSA_.kd
    .uniform_work_group_size: 1
    .uses_dynamic_stack: false
    .vgpr_count:     124
    .vgpr_spill_count: 0
    .wavefront_size: 64
  - .agpr_count:     0
    .args:
      - .actual_access:  read_only
        .address_space:  global
        .offset:         0
        .size:           8
        .value_kind:     global_buffer
      - .actual_access:  read_only
        .address_space:  global
        .offset:         8
        .size:           8
        .value_kind:     global_buffer
      - .actual_access:  read_only
        .address_space:  global
        .offset:         16
        .size:           8
        .value_kind:     global_buffer
      - .actual_access:  read_only
        .address_space:  global
        .offset:         24
        .size:           8
        .value_kind:     global_buffer
      - .actual_access:  read_only
        .address_space:  global
        .offset:         32
        .size:           8
        .value_kind:     global_buffer
      - .actual_access:  read_only
        .address_space:  global
        .offset:         40
        .size:           8
        .value_kind:     global_buffer
      - .actual_access:  write_only
        .address_space:  global
        .offset:         48
        .size:           8
        .value_kind:     global_buffer
      - .actual_access:  read_only
        .address_space:  global
        .offset:         56
        .size:           8
        .value_kind:     global_buffer
      - .actual_access:  read_only
        .address_space:  global
        .offset:         64
        .size:           8
        .value_kind:     global_buffer
      - .actual_access:  read_only
        .address_space:  global
        .offset:         72
        .size:           8
        .value_kind:     global_buffer
      - .actual_access:  read_only
        .address_space:  global
        .offset:         80
        .size:           8
        .value_kind:     global_buffer
      - .actual_access:  read_only
        .address_space:  global
        .offset:         88
        .size:           8
        .value_kind:     global_buffer
      - .actual_access:  read_only
        .address_space:  global
        .offset:         96
        .size:           8
        .value_kind:     global_buffer
      - .offset:         104
        .size:           4
        .value_kind:     hidden_block_count_x
      - .offset:         108
        .size:           4
        .value_kind:     hidden_block_count_y
      - .offset:         112
        .size:           4
        .value_kind:     hidden_block_count_z
      - .offset:         116
        .size:           2
        .value_kind:     hidden_group_size_x
      - .offset:         118
        .size:           2
        .value_kind:     hidden_group_size_y
      - .offset:         120
        .size:           2
        .value_kind:     hidden_group_size_z
      - .offset:         122
        .size:           2
        .value_kind:     hidden_remainder_x
      - .offset:         124
        .size:           2
        .value_kind:     hidden_remainder_y
      - .offset:         126
        .size:           2
        .value_kind:     hidden_remainder_z
      - .offset:         144
        .size:           8
        .value_kind:     hidden_global_offset_x
      - .offset:         152
        .size:           8
        .value_kind:     hidden_global_offset_y
      - .offset:         160
        .size:           8
        .value_kind:     hidden_global_offset_z
      - .offset:         168
        .size:           2
        .value_kind:     hidden_grid_dims
    .group_segment_fixed_size: 8704
    .kernarg_segment_align: 8
    .kernarg_segment_size: 360
    .language:       OpenCL C
    .language_version:
      - 2
      - 0
    .max_flat_workgroup_size: 256
    .name:           _Z5k_aggILi1ELi40ELi5ELi5ELb1EEvPKiPKtPKDF16_PKfS7_S7_PvS5_S7_S7_PDF16_PfSA_
    .private_segment_fixed_size: 0
    .sgpr_count:     46
    .sgpr_spill_count: 0
    .symbol:         _Z5k_aggILi1ELi40ELi5ELi5ELb1EEvPKiPKtPKDF16_PKfS7_S7_PvS5_S7_S7_PDF16_PfSA_.kd
    .uniform_work_group_size: 1
    .uses_dynamic_stack: false
    .vgpr_count:     76
    .vgpr_spill_count: 0
    .wavefront_size: 64
